# diff-attention: Q fragment LDS addresses formed once per unit instead of per tile
# speedup vs baseline: 1.0052x; 1.0052x over previous
.LBB0_564:
	s_xor_b64 s[12:13], s[14:15], -1
	s_and_b64 s[14:15], s[14:15], exec
	s_cselect_b32 s39, s31, s34
	s_mul_i32 s14, s39, 0x1a00
	v_mov_b32_e32 v128, v231
	s_add_u32 s16, s6, s14
	s_addc_u32 s17, s7, 0
	v_readfirstlane_b32 s18, v128
	v_lshlrev_b32_e32 v0, 3, v128
	s_ashr_i32 s14, s18, 6
	v_and_b32_e32 v129, 0x78, v0
	v_bfe_u32 v130, v128, 4, 2
	s_lshl_b32 s38, s14, 5
	v_lshlrev_b32_e32 v208, 1, v129
	v_or_b32_e32 v2, 4, v130
	v_or_b32_e32 v8, 8, v130
	v_or_b32_e32 v10, 12, v130
	v_lshl_add_u64 v[28:29], s[16:17], 0, v[208:209]
	v_or_b32_e32 v32, s38, v130
	v_or_b32_e32 v33, s38, v2
	v_or_b32_e32 v34, s38, v8
	v_or_b32_e32 v35, s38, v10
	v_mad_i64_i32 v[0:1], s[16:17], v32, s62, v[28:29]
	v_mad_i64_i32 v[4:5], s[16:17], v33, s62, v[28:29]
	v_mad_i64_i32 v[8:9], s[16:17], v34, s62, v[28:29]
	v_mad_i64_i32 v[12:13], s[16:17], v35, s62, v[28:29]
	global_load_dwordx4 v[0:3], v[0:1], off
	s_nop 0
	global_load_dwordx4 v[4:7], v[4:5], off
	s_nop 0
	global_load_dwordx4 v[8:11], v[8:9], off
	s_nop 0
	global_load_dwordx4 v[12:15], v[12:13], off
	v_or_b32_e32 v36, 16, v32
	v_mad_i64_i32 v[16:17], s[16:17], v36, s62, v[28:29]
	global_load_dwordx4 v[16:19], v[16:17], off
	v_or_b32_e32 v20, 20, v130
	v_or_b32_e32 v37, s38, v20
	v_mad_i64_i32 v[20:21], s[16:17], v37, s62, v[28:29]
	global_load_dwordx4 v[20:23], v[20:21], off
	v_or_b32_e32 v24, 24, v130
	v_or_b32_e32 v38, s38, v24
	v_mad_i64_i32 v[24:25], s[16:17], v38, s62, v[28:29]
	v_or_b32_e32 v30, 28, v130
	global_load_dwordx4 v[24:27], v[24:25], off
	v_or_b32_e32 v39, s38, v30
	v_mad_i64_i32 v[28:29], s[16:17], v39, s62, v[28:29]
	global_load_dwordx4 v[28:31], v[28:29], off
	v_xor_b32_e32 v40, v130, v128
	v_bitop3_b32 v41, v130, v128, 4 bitop3:0x36
	v_bitop3_b32 v42, v130, v128, 8 bitop3:0x36
	v_bitop3_b32 v43, v130, v128, 12 bitop3:0x36
	v_lshlrev_b32_e32 v40, 4, v40
	v_lshlrev_b32_e32 v41, 4, v41
	v_lshlrev_b32_e32 v42, 4, v42
	v_lshlrev_b32_e32 v43, 4, v43
	v_and_b32_e32 v40, 0xf0, v40
	v_lshlrev_b32_e32 v32, 8, v32
	v_and_b32_e32 v41, 0xf0, v41
	v_and_b32_e32 v42, 0xf0, v42
	v_and_b32_e32 v43, 0xf0, v43
	v_lshlrev_b32_e32 v33, 8, v33
	v_lshlrev_b32_e32 v34, 8, v34
	v_lshlrev_b32_e32 v35, 8, v35
	v_add3_u32 v32, s65, v32, v40
	s_and_b32 s16, s18, 0x3fffffc0
	v_add3_u32 v33, s65, v33, v41
	v_add3_u32 v34, s65, v34, v42
	v_add3_u32 v35, s65, v35, v43
	v_lshlrev_b32_e32 v36, 8, v36
	s_lshl_b32 s16, s16, 2
	s_add_i32 s40, s16, 0
	s_lshl_b32 s16, s14, 3
	v_bitop3_b32 v56, s16, v128, v130 bitop3:0x36
	v_or_b32_e32 v55, s16, v130
	v_lshlrev_b32_e32 v56, 3, v56
	v_mul_lo_u32 v57, v55, s96
	v_and_b32_e32 v133, 0x78, v56
	v_bitop3_b32 v55, v55, v128, 4 bitop3:0x36
	v_lshlrev_b32_e32 v132, 5, v130
	v_or_b32_e32 v56, v133, v57
	v_lshlrev_b32_e32 v55, 3, v55
	v_lshlrev_b32_e32 v208, 1, v56
	v_bitop3_b32 v56, v57, v132, v129 bitop3:0xf6
	v_add_u32_e32 v57, 0x3400, v57
	s_waitcnt vmcnt(7)
	ds_write_b128 v32, v[0:3]
	s_waitcnt vmcnt(6)
	ds_write_b128 v33, v[4:7]
	s_waitcnt vmcnt(5)
	ds_write_b128 v34, v[8:11]
	s_waitcnt vmcnt(4)
	ds_write_b128 v35, v[12:15]
	v_bitop3_b32 v1, v130, v128, 20 bitop3:0x36
	v_add3_u32 v0, s65, v36, v40
	v_lshlrev_b32_e32 v1, 4, v1
	s_waitcnt vmcnt(3)
	ds_write_b128 v0, v[16:19]
	v_lshlrev_b32_e32 v0, 8, v37
	v_and_b32_e32 v1, 0xf0, v1
	v_add3_u32 v0, s65, v0, v1
	v_bitop3_b32 v1, v130, v128, 24 bitop3:0x36
	v_lshlrev_b32_e32 v1, 4, v1
	s_waitcnt vmcnt(2)
	ds_write_b128 v0, v[20:23]
	v_lshlrev_b32_e32 v0, 8, v38
	v_and_b32_e32 v1, 0xf0, v1
	v_add3_u32 v0, s65, v0, v1
	v_bitop3_b32 v1, v130, v128, 28 bitop3:0x36
	v_lshlrev_b32_e32 v1, 4, v1
	v_and_b32_e32 v134, 0x78, v55
	s_waitcnt vmcnt(1)
	ds_write_b128 v0, v[24:27]
	v_lshlrev_b32_e32 v0, 8, v39
	v_and_b32_e32 v1, 0xf0, v1
	v_or_b32_e32 v55, v134, v57
	s_lshl_b32 s16, s14, 11
	v_add3_u32 v0, s65, v0, v1
	v_lshlrev_b32_e32 v56, 1, v56
	v_lshlrev_b32_e32 v58, 1, v55
	v_bitop3_b32 v55, v57, v132, v129 bitop3:0xf6
	v_lshl_add_u64 v[62:63], s[6:7], 0, v[208:209]
	s_add_i32 s44, s16, 0
	v_mov_b32_e32 v57, v209
	s_waitcnt vmcnt(0)
	ds_write_b128 v0, v[28:31]
	v_mov_b32_e32 v64, v209
	v_mov_b32_e32 v32, v209
	v_mov_b32_e32 v16, v209
	v_mov_b32_e32 v0, v209
	v_mov_b32_e32 v112, v209
	v_mov_b32_e32 v96, v209
	v_mov_b32_e32 v80, v209
	v_mov_b32_e32 v48, v209
	v_lshl_add_u64 v[62:63], v[62:63], 0, s[86:87]
	s_mov_b32 m0, s44
	v_lshl_add_u64 v[56:57], s[6:7], 0, v[56:57]
	global_load_lds_dwordx4 v[62:63], off
	v_lshl_add_u64 v[56:57], v[56:57], 0, s[88:89]
	s_add_i32 m0, s44, 0x8000
	v_mov_b32_e32 v59, v209
	global_load_lds_dwordx4 v[56:57], off
	v_lshl_add_u64 v[56:57], s[6:7], 0, v[58:59]
	v_lshlrev_b32_e32 v60, 1, v55
	v_lshl_add_u64 v[56:57], v[56:57], 0, s[86:87]
	s_add_i32 m0, s44, 0x400
	v_mov_b32_e32 v61, v209
	global_load_lds_dwordx4 v[56:57], off
	v_lshl_add_u64 v[56:57], s[6:7], 0, v[60:61]
	v_lshl_add_u64 v[56:57], v[56:57], 0, s[88:89]
	s_add_i32 m0, s44, 0x8400
	v_bfe_u32 v135, v128, 5, 1
	global_load_lds_dwordx4 v[56:57], off
	v_and_b32_e32 v235, 63, v128
	v_and_b32_e32 v131, 31, v128
	v_and_b32_e32 v136, 15, v128
	v_bfe_u32 v137, v128, 2, 2
	v_and_b32_e32 v139, 16, v128
	v_lshlrev_b32_e32 v140, 2, v128
	v_bitop3_b32 v128, v135, v128, 15 bitop3:0x78
	v_lshlrev_b32_e32 v240, 4, v128
	v_bitop3_b32 v128, v135, v136, 2 bitop3:0x36
	v_lshlrev_b32_e32 v241, 4, v128
	v_bitop3_b32 v128, v135, v136, 4 bitop3:0x36
	v_lshlrev_b32_e32 v242, 4, v128
	v_bitop3_b32 v128, v135, v136, 6 bitop3:0x36
	v_lshlrev_b32_e32 v243, 4, v128
	v_bitop3_b32 v128, v135, v136, 8 bitop3:0x36
	v_lshlrev_b32_e32 v244, 4, v128
	v_bitop3_b32 v128, v135, v136, 10 bitop3:0x36
	v_lshlrev_b32_e32 v245, 4, v128
	v_bitop3_b32 v128, v135, v136, 12 bitop3:0x36
	s_add_i32 s16, s38, s39
	v_lshlrev_b32_e32 v246, 4, v128
	v_bitop3_b32 v128, v135, v136, 14 bitop3:0x36
	v_or_b32_e32 v44, s38, v131
	s_add_i32 s40, s40, 0x10000
	v_lshl_add_u32 v237, v131, 8, 0
	v_lshlrev_b32_e32 v247, 4, v128
	v_lshlrev_b32_e32 v128, 4, v135
	v_add_lshl_u32 v131, s16, v131, 2
	v_add_u32_e32 v249, s40, v128
	v_sub_u32_e32 v128, v128, v131
	s_mulk_i32 s14, 0x6800
	v_add_u32_e32 v250, s97, v128
	v_mov_b32_e32 v128, s14
	v_mad_u32_u24 v128, v130, s96, v128
	v_or_b32_e32 v131, v128, v133
	s_addk_i32 s14, 0x3400
	v_lshlrev_b32_e32 v208, 1, v131
	v_mov_b32_e32 v131, s14
	v_mad_u32_u24 v130, v130, s96, v131
	v_or_b32_e32 v130, v130, v134
	s_ashr_i32 s17, s16, 31
	v_lshl_add_u64 v[210:211], s[8:9], 0, v[208:209]
	v_lshlrev_b32_e32 v208, 1, v130
	v_bitop3_b32 v128, v132, v128, v129 bitop3:0xde
	s_lshr_b32 s15, s39, 6
	s_lshr_b32 s17, s17, 26
	v_lshlrev_b32_e32 v138, 8, v137
	v_and_or_b32 v139, v140, 12, v139
	v_lshl_add_u64 v[216:217], s[8:9], 0, v[208:209]
	v_lshlrev_b32_e32 v208, 1, v128
	s_add_i32 s42, s15, 4
	s_add_i32 s17, s16, s17
	v_lshl_or_b32 v138, v135, 10, v138
	v_lshlrev_b32_e32 v139, 1, v139
	s_mul_i32 s15, s15, 0x68000
	v_lshl_add_u64 v[218:219], s[10:11], 0, v[208:209]
	v_add_u32_e32 v208, 0x6800, v208
	s_mov_b32 s41, 1
	v_lshl_add_u32 v236, v44, 8, s65
	s_mov_b32 s43, 0
	v_mov_b32_e32 v65, v64
	v_mov_b32_e32 v66, v64
	v_mov_b32_e32 v67, v64
	v_mov_b32_e32 v68, v64
	v_mov_b32_e32 v69, v64
	v_mov_b32_e32 v70, v64
	v_mov_b32_e32 v71, v64
	v_mov_b32_e32 v72, v64
	v_mov_b32_e32 v73, v64
	v_mov_b32_e32 v74, v64
	v_mov_b32_e32 v75, v64
	v_mov_b32_e32 v76, v64
	v_mov_b32_e32 v77, v64
	v_mov_b32_e32 v78, v64
	v_mov_b32_e32 v79, v64
	v_mov_b32_e32 v33, v32
	v_mov_b32_e32 v34, v32
	v_mov_b32_e32 v35, v32
	v_mov_b32_e32 v36, v32
	v_mov_b32_e32 v37, v32
	v_mov_b32_e32 v38, v32
	v_mov_b32_e32 v39, v32
	v_mov_b32_e32 v40, v32
	v_mov_b32_e32 v41, v32
	v_mov_b32_e32 v42, v32
	v_mov_b32_e32 v43, v32
	v_mov_b32_e32 v44, v32
	v_mov_b32_e32 v45, v32
	v_mov_b32_e32 v46, v32
	v_mov_b32_e32 v47, v32
	v_mov_b32_e32 v17, v16
	v_mov_b32_e32 v18, v16
	v_mov_b32_e32 v19, v16
	v_mov_b32_e32 v20, v16
	v_mov_b32_e32 v21, v16
	v_mov_b32_e32 v22, v16
	v_mov_b32_e32 v23, v16
	v_mov_b32_e32 v24, v16
	v_mov_b32_e32 v25, v16
	v_mov_b32_e32 v26, v16
	v_mov_b32_e32 v27, v16
	v_mov_b32_e32 v28, v16
	v_mov_b32_e32 v29, v16
	v_mov_b32_e32 v30, v16
	v_mov_b32_e32 v31, v16
	v_mov_b32_e32 v1, v0
	v_mov_b32_e32 v2, v0
	v_mov_b32_e32 v3, v0
	v_mov_b32_e32 v4, v0
	v_mov_b32_e32 v5, v0
	v_mov_b32_e32 v6, v0
	v_mov_b32_e32 v7, v0
	v_mov_b32_e32 v8, v0
	v_mov_b32_e32 v9, v0
	v_mov_b32_e32 v10, v0
	v_mov_b32_e32 v11, v0
	v_mov_b32_e32 v12, v0
	v_mov_b32_e32 v13, v0
	v_mov_b32_e32 v14, v0
	v_mov_b32_e32 v15, v0
	v_mov_b32_e32 v113, v112
	v_mov_b32_e32 v114, v112
	v_mov_b32_e32 v115, v112
	v_mov_b32_e32 v116, v112
	v_mov_b32_e32 v117, v112
	v_mov_b32_e32 v118, v112
	v_mov_b32_e32 v119, v112
	v_mov_b32_e32 v120, v112
	v_mov_b32_e32 v121, v112
	v_mov_b32_e32 v122, v112
	v_mov_b32_e32 v123, v112
	v_mov_b32_e32 v124, v112
	v_mov_b32_e32 v125, v112
	v_mov_b32_e32 v126, v112
	v_mov_b32_e32 v127, v112
	v_mov_b32_e32 v97, v96
	v_mov_b32_e32 v98, v96
	v_mov_b32_e32 v99, v96
	v_mov_b32_e32 v100, v96
	v_mov_b32_e32 v101, v96
	v_mov_b32_e32 v102, v96
	v_mov_b32_e32 v103, v96
	v_mov_b32_e32 v104, v96
	v_mov_b32_e32 v105, v96
	v_mov_b32_e32 v106, v96
	v_mov_b32_e32 v107, v96
	v_mov_b32_e32 v108, v96
	v_mov_b32_e32 v109, v96
	v_mov_b32_e32 v110, v96
	v_mov_b32_e32 v111, v96
	v_mov_b32_e32 v81, v80
	v_mov_b32_e32 v82, v80
	v_mov_b32_e32 v83, v80
	v_mov_b32_e32 v84, v80
	v_mov_b32_e32 v85, v80
	v_mov_b32_e32 v86, v80
	v_mov_b32_e32 v87, v80
	v_mov_b32_e32 v88, v80
	v_mov_b32_e32 v89, v80
	v_mov_b32_e32 v90, v80
	v_mov_b32_e32 v91, v80
	v_mov_b32_e32 v92, v80
	v_mov_b32_e32 v93, v80
	v_mov_b32_e32 v94, v80
	v_mov_b32_e32 v95, v80
	v_mov_b32_e32 v49, v48
	v_mov_b32_e32 v50, v48
	v_mov_b32_e32 v51, v48
	v_mov_b32_e32 v52, v48
	v_mov_b32_e32 v53, v48
	v_mov_b32_e32 v54, v48
	v_mov_b32_e32 v55, v48
	v_mov_b32_e32 v56, v48
	v_mov_b32_e32 v57, v48
	v_mov_b32_e32 v58, v48
	v_mov_b32_e32 v59, v48
	v_mov_b32_e32 v60, v48
	v_mov_b32_e32 v61, v48
	v_mov_b32_e32 v62, v48
	v_mov_b32_e32 v63, v48
	s_ashr_i32 s45, s17, 6
	v_add3_u32 v238, 0, v138, v139
	v_lshl_add_u32 v239, v235, 2, s40
	v_lshlrev_b32_e32 v248, 6, v137
	s_add_u32 s46, s15, 0x1a0000
	v_lshl_add_u64 v[220:221], s[10:11], 0, v[208:209]
	s_sub_i32 s47, 0, s16
	v_mov_b32_e32 v226, 0xff800000
	v_mov_b32_e32 v251, 0
	s_mov_b64 s[14:15], 0
	v_mov_b32_e32 v208, 0
	v_mov_b32_e32 v227, 0xff800000
	s_add_i32 m0, s44, 0x4000
	s_nop 0
	global_load_lds_dwordx4 v[210:211], off
	s_add_i32 m0, s44, 0x4400
	s_nop 0
	global_load_lds_dwordx4 v[216:217], off
	s_waitcnt vmcnt(0) lgkmcnt(0)
	s_barrier
	v_add_u32_e32 v240, v236, v240
	v_add_u32_e32 v241, v236, v241
	v_add_u32_e32 v242, v236, v242
	v_add_u32_e32 v243, v236, v243
	v_add_u32_e32 v244, v236, v244
	v_add_u32_e32 v245, v236, v245
	v_add_u32_e32 v246, v236, v246
	v_add_u32_e32 v247, v236, v247
	v_sub_u32_e32 v237, v237, v236
	s_mov_b32 s48, 0
	v_mov_b32_e32 v228, s64
	ds_read_b32 v229, v228
	v_add3_u32 v254, v237, v240, s48
	ds_read_b128 v[128:131], v254
	ds_read_b128 v[132:135], v254 offset:8192
	ds_read_b128 v[136:139], v240
	v_add3_u32 v254, v237, v241, s48
	ds_read_b128 v[140:143], v254
	ds_read_b128 v[144:147], v254 offset:8192
	ds_read_b128 v[148:151], v241
	v_add3_u32 v254, v237, v242, s48
	ds_read_b128 v[152:155], v254
	ds_read_b128 v[156:159], v254 offset:8192
	ds_read_b128 v[192:195], v242
	v_add3_u32 v254, v237, v243, s48
	ds_read_b128 v[196:199], v254
	ds_read_b128 v[200:203], v254 offset:8192
	ds_read_b128 v[204:207], v243
	s_waitcnt lgkmcnt(9)
	v_mfma_f32_32x32x16_bf16 v[160:175], v[128:131], v[136:139], 0
	v_mfma_f32_32x32x16_bf16 v[176:191], v[132:135], v[136:139], 0
	s_waitcnt lgkmcnt(6)
	v_mfma_f32_32x32x16_bf16 v[160:175], v[140:143], v[148:151], v[160:175]
	v_mfma_f32_32x32x16_bf16 v[176:191], v[144:147], v[148:151], v[176:191]
	s_waitcnt lgkmcnt(3)
	v_mfma_f32_32x32x16_bf16 v[160:175], v[152:155], v[192:195], v[160:175]
	v_mfma_f32_32x32x16_bf16 v[176:191], v[156:159], v[192:195], v[176:191]
	s_waitcnt lgkmcnt(0)
	v_mfma_f32_32x32x16_bf16 v[160:175], v[196:199], v[204:207], v[160:175]
	v_mfma_f32_32x32x16_bf16 v[176:191], v[200:203], v[204:207], v[176:191]
	v_readfirstlane_b32 s50, v229

.Lattn_noresc0_a:
	ds_read_b64_tr_b16 v[156:157], v215 offset:36864
	ds_read_b64_tr_b16 v[158:159], v215 offset:38912
	ds_read_b64_tr_b16 v[192:193], v212 offset:40960
	ds_read_b64_tr_b16 v[194:195], v212 offset:43008
	ds_read_b64_tr_b16 v[196:197], v213 offset:40960
	ds_read_b64_tr_b16 v[198:199], v213 offset:43008
	ds_read_b64_tr_b16 v[200:201], v214 offset:40960
	ds_read_b64_tr_b16 v[202:203], v214 offset:43008
	v_sub_f32_e32 v160, v160, v229
	v_sub_f32_e32 v161, v161, v229
	v_sub_f32_e32 v162, v162, v229
	s_waitcnt lgkmcnt(12)
	v_mfma_f32_32x32x16_bf16 v[112:127], v[132:135], v[144:147], v[112:127]
	ds_read_b64_tr_b16 v[204:205], v215 offset:40960
	ds_read_b64_tr_b16 v[206:207], v215 offset:43008
	v_sub_f32_e32 v163, v163, v229
	v_exp_f32_e32 v160, v160
	v_exp_f32_e32 v161, v161
	v_exp_f32_e32 v162, v162
	v_exp_f32_e32 v163, v163
	s_waitcnt lgkmcnt(12)
	v_mfma_f32_32x32x16_bf16 v[96:111], v[132:135], v[148:151], v[96:111]
	ds_read_b64_tr_b16 v[144:145], v212 offset:45056
	ds_read_b64_tr_b16 v[146:147], v212 offset:47104
	v_add_f32_e32 v254, v160, v161
	v_add_f32_e32 v254, v254, v162
	v_add_f32_e32 v254, v254, v163
	v_sub_f32_e32 v164, v164, v229
	v_sub_f32_e32 v165, v165, v229
	s_waitcnt lgkmcnt(12)
	v_mfma_f32_32x32x16_bf16 v[80:95], v[132:135], v[152:155], v[80:95]
	ds_read_b64_tr_b16 v[148:149], v213 offset:45056
	ds_read_b64_tr_b16 v[150:151], v213 offset:47104
	v_sub_f32_e32 v166, v166, v229
	v_sub_f32_e32 v167, v167, v229
	v_exp_f32_e32 v164, v164
	v_exp_f32_e32 v165, v165
	v_exp_f32_e32 v166, v166
	s_waitcnt lgkmcnt(12)
	v_mfma_f32_32x32x16_bf16 v[48:63], v[132:135], v[156:159], v[48:63]
	ds_read_b64_tr_b16 v[152:153], v214 offset:45056
	ds_read_b64_tr_b16 v[154:155], v214 offset:47104
	v_exp_f32_e32 v167, v167
	v_add_f32_e32 v254, v254, v164
	v_add_f32_e32 v254, v254, v165
	v_add_f32_e32 v254, v254, v166
	v_add_f32_e32 v254, v254, v167
	s_waitcnt lgkmcnt(12)
	v_mfma_f32_32x32x16_bf16 v[112:127], v[136:139], v[192:195], v[112:127]
	ds_read_b64_tr_b16 v[156:157], v215 offset:45056
	ds_read_b64_tr_b16 v[158:159], v215 offset:47104
	v_cvt_pk_bf16_f32 v160, v160, v161
	v_cvt_pk_bf16_f32 v161, v162, v163
	v_sub_f32_e32 v168, v168, v229
	v_sub_f32_e32 v169, v169, v229
	v_sub_f32_e32 v170, v170, v229
	s_waitcnt lgkmcnt(12)
	v_mfma_f32_32x32x16_bf16 v[96:111], v[136:139], v[196:199], v[96:111]
	ds_read_b128 v[192:195], v244
	v_sub_f32_e32 v171, v171, v229
	v_exp_f32_e32 v168, v168
	v_exp_f32_e32 v169, v169
	v_exp_f32_e32 v170, v170
	v_exp_f32_e32 v171, v171
	s_waitcnt lgkmcnt(11)
	v_mfma_f32_32x32x16_bf16 v[80:95], v[136:139], v[200:203], v[80:95]
	v_add3_u32 v230, v237, v244, s48
	ds_read_b128 v[196:199], v230
	ds_read_b128 v[200:203], v230 offset:8192
	v_add_f32_e32 v254, v254, v168
	v_add_f32_e32 v254, v254, v169
	v_add_f32_e32 v254, v254, v170
	v_add_f32_e32 v254, v254, v171
	v_cvt_pk_bf16_f32 v162, v164, v165
	s_waitcnt lgkmcnt(11)
	v_mfma_f32_32x32x16_bf16 v[48:63], v[136:139], v[204:207], v[48:63]
	v_cvt_pk_bf16_f32 v163, v166, v167
	v_sub_f32_e32 v172, v172, v229
	v_sub_f32_e32 v173, v173, v229
	v_sub_f32_e32 v174, v174, v229
	v_sub_f32_e32 v175, v175, v229
	s_waitcnt lgkmcnt(9)
	v_mfma_f32_32x32x16_bf16 v[112:127], v[140:143], v[144:147], v[112:127]
	ds_read_b128 v[204:207], v245
	v_exp_f32_e32 v172, v172
	v_exp_f32_e32 v173, v173
	v_exp_f32_e32 v174, v174
	v_exp_f32_e32 v175, v175
	v_add_f32_e32 v254, v254, v172
	s_waitcnt lgkmcnt(8)
	v_mfma_f32_32x32x16_bf16 v[96:111], v[140:143], v[148:151], v[96:111]
	v_add_f32_e32 v254, v254, v173
	v_add_f32_e32 v254, v254, v174
	v_add_f32_e32 v254, v254, v175
	v_cvt_pk_bf16_f32 v164, v168, v169
	v_cvt_pk_bf16_f32 v165, v170, v171
	s_waitcnt lgkmcnt(6)
	v_mfma_f32_32x32x16_bf16 v[80:95], v[140:143], v[152:155], v[80:95]
	v_sub_f32_e32 v176, v176, v229
	v_sub_f32_e32 v177, v177, v229
	v_sub_f32_e32 v178, v178, v229
	v_sub_f32_e32 v179, v179, v229
	v_exp_f32_e32 v176, v176
	v_exp_f32_e32 v177, v177
	s_waitcnt lgkmcnt(4)
	v_mfma_f32_32x32x16_bf16 v[48:63], v[140:143], v[156:159], v[48:63]
	v_exp_f32_e32 v178, v178
	v_exp_f32_e32 v179, v179
	v_add_f32_e32 v255, v176, v177
	v_add_f32_e32 v255, v255, v178
	v_add_f32_e32 v255, v255, v179
	s_waitcnt lgkmcnt(2)
	v_mfma_f32_32x32x16_bf16 v[128:143], v[196:199], v[192:195], 0
	v_cvt_pk_bf16_f32 v166, v172, v173
	v_cvt_pk_bf16_f32 v167, v174, v175
	v_sub_f32_e32 v180, v180, v229
	v_sub_f32_e32 v181, v181, v229
	v_sub_f32_e32 v182, v182, v229
	s_waitcnt lgkmcnt(1)
	v_mfma_f32_32x32x16_bf16 v[144:159], v[200:203], v[192:195], 0
	v_add3_u32 v230, v237, v245, s48
	ds_read_b128 v[196:199], v230
	ds_read_b128 v[200:203], v230 offset:8192
	ds_read_b128 v[192:195], v246
	v_sub_f32_e32 v183, v183, v229
	v_exp_f32_e32 v180, v180
	v_exp_f32_e32 v181, v181
	v_exp_f32_e32 v182, v182
	v_exp_f32_e32 v183, v183
	s_waitcnt lgkmcnt(2)
	v_mfma_f32_32x32x16_bf16 v[128:143], v[196:199], v[204:207], v[128:143]
	v_add_f32_e32 v255, v255, v180
	v_add_f32_e32 v255, v255, v181
	v_add_f32_e32 v255, v255, v182
	v_add_f32_e32 v255, v255, v183
	v_cvt_pk_bf16_f32 v168, v176, v177
	s_waitcnt lgkmcnt(1)
	v_mfma_f32_32x32x16_bf16 v[144:159], v[200:203], v[204:207], v[144:159]
	v_add3_u32 v230, v237, v246, s48
	ds_read_b128 v[196:199], v230
	ds_read_b128 v[200:203], v230 offset:8192
	ds_read_b128 v[204:207], v247
	v_cvt_pk_bf16_f32 v169, v178, v179
	v_sub_f32_e32 v184, v184, v229
	v_sub_f32_e32 v185, v185, v229
	v_sub_f32_e32 v186, v186, v229
	v_sub_f32_e32 v187, v187, v229
	s_waitcnt lgkmcnt(2)
	v_mfma_f32_32x32x16_bf16 v[128:143], v[196:199], v[192:195], v[128:143]
	v_exp_f32_e32 v184, v184
	v_exp_f32_e32 v185, v185
	v_exp_f32_e32 v186, v186
	v_exp_f32_e32 v187, v187
	v_add_f32_e32 v255, v255, v184
	s_waitcnt lgkmcnt(1)
	v_mfma_f32_32x32x16_bf16 v[144:159], v[200:203], v[192:195], v[144:159]
	v_add3_u32 v230, v237, v247, s48
	ds_read_b128 v[196:199], v230
	ds_read_b128 v[200:203], v230 offset:8192
	v_add_f32_e32 v255, v255, v185
	v_add_f32_e32 v255, v255, v186
	v_add_f32_e32 v255, v255, v187
	v_cvt_pk_bf16_f32 v170, v180, v181
	v_cvt_pk_bf16_f32 v171, v182, v183
	s_waitcnt lgkmcnt(1)
	v_mfma_f32_32x32x16_bf16 v[128:143], v[196:199], v[204:207], v[128:143]
	v_sub_f32_e32 v188, v188, v229
	v_sub_f32_e32 v189, v189, v229
	v_sub_f32_e32 v190, v190, v229
	v_sub_f32_e32 v191, v191, v229
	v_exp_f32_e32 v188, v188
	s_waitcnt lgkmcnt(0)
	v_mfma_f32_32x32x16_bf16 v[144:159], v[200:203], v[204:207], v[144:159]
	v_exp_f32_e32 v189, v189
	v_exp_f32_e32 v190, v190
	v_exp_f32_e32 v191, v191
	v_add_f32_e32 v255, v255, v188
	v_add_f32_e32 v255, v255, v189
	v_add_f32_e32 v255, v255, v190
	v_add_f32_e32 v255, v255, v191
	v_cvt_pk_bf16_f32 v172, v184, v185
	v_cvt_pk_bf16_f32 v173, v186, v187
	v_cvt_pk_bf16_f32 v174, v188, v189
	v_cvt_pk_bf16_f32 v175, v190, v191
	v_add_f32_e32 v254, v254, v255
	v_mov_b32_e32 v255, v254
	s_nop 1
	v_permlane32_swap_b32_e32 v254, v255
	v_add_f32_e32 v254, v254, v255
	v_fma_f32 v251, v251, v228, v254
	s_branch .Lattn_mid

.Lattn_noresc0_b:
	ds_read_b128 v[192:195], v244
	v_add3_u32 v230, v237, v244, s48
	ds_read_b128 v[196:199], v230
	ds_read_b128 v[200:203], v230 offset:8192
	ds_read_b128 v[204:207], v245
	v_sub_f32_e32 v160, v160, v229
	v_sub_f32_e32 v161, v161, v229
	v_sub_f32_e32 v162, v162, v229
	s_waitcnt lgkmcnt(2)
	v_mfma_f32_32x32x16_bf16 v[128:143], v[196:199], v[192:195], 0
	v_sub_f32_e32 v163, v163, v229
	v_exp_f32_e32 v160, v160
	v_exp_f32_e32 v161, v161
	v_exp_f32_e32 v162, v162
	v_exp_f32_e32 v163, v163
	v_add_f32_e32 v254, v160, v161
	v_add_f32_e32 v254, v254, v162
	v_add_f32_e32 v254, v254, v163
	v_sub_f32_e32 v164, v164, v229
	v_sub_f32_e32 v165, v165, v229
	v_sub_f32_e32 v166, v166, v229
	v_sub_f32_e32 v167, v167, v229
	v_exp_f32_e32 v164, v164
	s_waitcnt lgkmcnt(1)
	v_mfma_f32_32x32x16_bf16 v[144:159], v[200:203], v[192:195], 0
	v_add3_u32 v230, v237, v245, s48
	ds_read_b128 v[196:199], v230
	ds_read_b128 v[200:203], v230 offset:8192
	ds_read_b128 v[192:195], v246
	v_exp_f32_e32 v165, v165
	v_exp_f32_e32 v166, v166
	v_exp_f32_e32 v167, v167
	v_add_f32_e32 v254, v254, v164
	v_add_f32_e32 v254, v254, v165
	v_add_f32_e32 v254, v254, v166
	v_add_f32_e32 v254, v254, v167
	v_cvt_pk_bf16_f32 v160, v160, v161
	v_cvt_pk_bf16_f32 v161, v162, v163
	v_sub_f32_e32 v168, v168, v229
	v_sub_f32_e32 v169, v169, v229
	v_sub_f32_e32 v170, v170, v229
	v_sub_f32_e32 v171, v171, v229
	v_exp_f32_e32 v168, v168
	s_waitcnt lgkmcnt(2)
	v_mfma_f32_32x32x16_bf16 v[128:143], v[196:199], v[204:207], v[128:143]
	v_exp_f32_e32 v169, v169
	v_exp_f32_e32 v170, v170
	v_exp_f32_e32 v171, v171
	v_add_f32_e32 v254, v254, v168
	v_add_f32_e32 v254, v254, v169
	v_add_f32_e32 v254, v254, v170
	v_add_f32_e32 v254, v254, v171
	v_cvt_pk_bf16_f32 v162, v164, v165
	v_cvt_pk_bf16_f32 v163, v166, v167
	v_sub_f32_e32 v172, v172, v229
	v_sub_f32_e32 v173, v173, v229
	v_sub_f32_e32 v174, v174, v229
	v_sub_f32_e32 v175, v175, v229
	v_exp_f32_e32 v172, v172
	s_waitcnt lgkmcnt(1)
	v_mfma_f32_32x32x16_bf16 v[144:159], v[200:203], v[204:207], v[144:159]
	v_add3_u32 v230, v237, v246, s48
	ds_read_b128 v[196:199], v230
	ds_read_b128 v[200:203], v230 offset:8192
	ds_read_b128 v[204:207], v247
	v_exp_f32_e32 v173, v173
	v_exp_f32_e32 v174, v174
	v_exp_f32_e32 v175, v175
	v_add_f32_e32 v254, v254, v172
	v_add_f32_e32 v254, v254, v173
	v_add_f32_e32 v254, v254, v174
	v_add_f32_e32 v254, v254, v175
	v_cvt_pk_bf16_f32 v164, v168, v169
	v_cvt_pk_bf16_f32 v165, v170, v171
	v_sub_f32_e32 v176, v176, v229
	v_sub_f32_e32 v177, v177, v229
	v_sub_f32_e32 v178, v178, v229
	v_sub_f32_e32 v179, v179, v229
	v_exp_f32_e32 v176, v176
	s_waitcnt lgkmcnt(2)
	v_mfma_f32_32x32x16_bf16 v[128:143], v[196:199], v[192:195], v[128:143]
	v_exp_f32_e32 v177, v177
	v_exp_f32_e32 v178, v178
	v_exp_f32_e32 v179, v179
	v_add_f32_e32 v255, v176, v177
	v_add_f32_e32 v255, v255, v178
	v_add_f32_e32 v255, v255, v179
	v_cvt_pk_bf16_f32 v166, v172, v173
	v_cvt_pk_bf16_f32 v167, v174, v175
	v_sub_f32_e32 v180, v180, v229
	v_sub_f32_e32 v181, v181, v229
	v_sub_f32_e32 v182, v182, v229
	v_sub_f32_e32 v183, v183, v229
	v_exp_f32_e32 v180, v180
	v_exp_f32_e32 v181, v181
	s_waitcnt lgkmcnt(1)
	v_mfma_f32_32x32x16_bf16 v[144:159], v[200:203], v[192:195], v[144:159]
	v_add3_u32 v230, v237, v247, s48
	ds_read_b128 v[196:199], v230
	ds_read_b128 v[200:203], v230 offset:8192
	v_exp_f32_e32 v182, v182
	v_exp_f32_e32 v183, v183
	v_add_f32_e32 v255, v255, v180
	v_add_f32_e32 v255, v255, v181
	v_add_f32_e32 v255, v255, v182
	v_add_f32_e32 v255, v255, v183
	v_cvt_pk_bf16_f32 v168, v176, v177
	v_cvt_pk_bf16_f32 v169, v178, v179
	v_sub_f32_e32 v184, v184, v229
	v_sub_f32_e32 v185, v185, v229
	v_sub_f32_e32 v186, v186, v229
	v_sub_f32_e32 v187, v187, v229
	v_exp_f32_e32 v184, v184
	s_waitcnt lgkmcnt(1)
	v_mfma_f32_32x32x16_bf16 v[128:143], v[196:199], v[204:207], v[128:143]
	v_exp_f32_e32 v185, v185
	v_exp_f32_e32 v186, v186
	v_exp_f32_e32 v187, v187
	v_add_f32_e32 v255, v255, v184
	v_add_f32_e32 v255, v255, v185
	v_add_f32_e32 v255, v255, v186
	v_add_f32_e32 v255, v255, v187
	v_cvt_pk_bf16_f32 v170, v180, v181
	v_cvt_pk_bf16_f32 v171, v182, v183
	v_sub_f32_e32 v188, v188, v229
	v_sub_f32_e32 v189, v189, v229
	v_sub_f32_e32 v190, v190, v229
	v_sub_f32_e32 v191, v191, v229
	v_exp_f32_e32 v188, v188
	s_waitcnt lgkmcnt(0)
	v_mfma_f32_32x32x16_bf16 v[144:159], v[200:203], v[204:207], v[144:159]
	v_exp_f32_e32 v189, v189
	v_exp_f32_e32 v190, v190
	v_exp_f32_e32 v191, v191
	v_add_f32_e32 v255, v255, v188
	v_add_f32_e32 v255, v255, v189
	v_add_f32_e32 v255, v255, v190
	v_add_f32_e32 v255, v255, v191
	v_cvt_pk_bf16_f32 v172, v184, v185
	v_cvt_pk_bf16_f32 v173, v186, v187
	v_cvt_pk_bf16_f32 v174, v188, v189
	v_cvt_pk_bf16_f32 v175, v190, v191
	v_add_f32_e32 v254, v254, v255
	v_mov_b32_e32 v255, v254
	s_nop 1
	v_permlane32_swap_b32_e32 v254, v255
	v_add_f32_e32 v254, v254, v255
	v_fma_f32 v251, v251, v228, v254
	s_branch .Lattn_mid

.Lattn_noresc1_c:
	ds_read_b64_tr_b16 v[188:189], v215 offset:36864
	ds_read_b64_tr_b16 v[190:191], v215 offset:38912
	ds_read_b64_tr_b16 v[192:193], v212 offset:40960
	ds_read_b64_tr_b16 v[194:195], v212 offset:43008
	ds_read_b64_tr_b16 v[196:197], v213 offset:40960
	ds_read_b64_tr_b16 v[198:199], v213 offset:43008
	ds_read_b64_tr_b16 v[200:201], v214 offset:40960
	ds_read_b64_tr_b16 v[202:203], v214 offset:43008
	v_sub_f32_e32 v128, v128, v229
	v_sub_f32_e32 v129, v129, v229
	v_sub_f32_e32 v130, v130, v229
	s_waitcnt lgkmcnt(12)
	v_mfma_f32_32x32x16_bf16 v[64:79], v[164:167], v[176:179], v[64:79]
	ds_read_b64_tr_b16 v[204:205], v215 offset:40960
	ds_read_b64_tr_b16 v[206:207], v215 offset:43008
	v_sub_f32_e32 v131, v131, v229
	v_exp_f32_e32 v128, v128
	v_exp_f32_e32 v129, v129
	v_exp_f32_e32 v130, v130
	v_exp_f32_e32 v131, v131
	s_waitcnt lgkmcnt(12)
	v_mfma_f32_32x32x16_bf16 v[32:47], v[164:167], v[180:183], v[32:47]
	ds_read_b64_tr_b16 v[176:177], v212 offset:45056
	ds_read_b64_tr_b16 v[178:179], v212 offset:47104
	v_add_f32_e32 v254, v128, v129
	v_add_f32_e32 v254, v254, v130
	v_add_f32_e32 v254, v254, v131
	v_sub_f32_e32 v132, v132, v229
	v_sub_f32_e32 v133, v133, v229
	s_waitcnt lgkmcnt(12)
	v_mfma_f32_32x32x16_bf16 v[16:31], v[164:167], v[184:187], v[16:31]
	ds_read_b64_tr_b16 v[180:181], v213 offset:45056
	ds_read_b64_tr_b16 v[182:183], v213 offset:47104
	v_sub_f32_e32 v134, v134, v229
	v_sub_f32_e32 v135, v135, v229
	v_exp_f32_e32 v132, v132
	v_exp_f32_e32 v133, v133
	v_exp_f32_e32 v134, v134
	s_waitcnt lgkmcnt(12)
	v_mfma_f32_32x32x16_bf16 v[0:15], v[164:167], v[188:191], v[0:15]
	ds_read_b64_tr_b16 v[184:185], v214 offset:45056
	ds_read_b64_tr_b16 v[186:187], v214 offset:47104
	v_exp_f32_e32 v135, v135
	v_add_f32_e32 v254, v254, v132
	v_add_f32_e32 v254, v254, v133
	v_add_f32_e32 v254, v254, v134
	v_add_f32_e32 v254, v254, v135
	s_waitcnt lgkmcnt(12)
	v_mfma_f32_32x32x16_bf16 v[64:79], v[168:171], v[192:195], v[64:79]
	ds_read_b64_tr_b16 v[188:189], v215 offset:45056
	ds_read_b64_tr_b16 v[190:191], v215 offset:47104
	v_cvt_pk_bf16_f32 v128, v128, v129
	v_cvt_pk_bf16_f32 v129, v130, v131
	v_sub_f32_e32 v136, v136, v229
	v_sub_f32_e32 v137, v137, v229
	v_sub_f32_e32 v138, v138, v229
	s_waitcnt lgkmcnt(12)
	v_mfma_f32_32x32x16_bf16 v[32:47], v[168:171], v[196:199], v[32:47]
	ds_read_b128 v[192:195], v240
	v_sub_f32_e32 v139, v139, v229
	v_exp_f32_e32 v136, v136
	v_exp_f32_e32 v137, v137
	v_exp_f32_e32 v138, v138
	v_exp_f32_e32 v139, v139
	s_waitcnt lgkmcnt(11)
	v_mfma_f32_32x32x16_bf16 v[16:31], v[168:171], v[200:203], v[16:31]
	v_add3_u32 v230, v237, v240, s51
	ds_read_b128 v[196:199], v230
	ds_read_b128 v[200:203], v230 offset:8192
	v_add_f32_e32 v254, v254, v136
	v_add_f32_e32 v254, v254, v137
	v_add_f32_e32 v254, v254, v138
	v_add_f32_e32 v254, v254, v139
	v_cvt_pk_bf16_f32 v130, v132, v133
	s_waitcnt lgkmcnt(11)
	v_mfma_f32_32x32x16_bf16 v[0:15], v[168:171], v[204:207], v[0:15]
	v_cvt_pk_bf16_f32 v131, v134, v135
	v_sub_f32_e32 v140, v140, v229
	v_sub_f32_e32 v141, v141, v229
	v_sub_f32_e32 v142, v142, v229
	v_sub_f32_e32 v143, v143, v229
	s_waitcnt lgkmcnt(9)
	v_mfma_f32_32x32x16_bf16 v[64:79], v[172:175], v[176:179], v[64:79]
	ds_read_b128 v[204:207], v241
	v_exp_f32_e32 v140, v140
	v_exp_f32_e32 v141, v141
	v_exp_f32_e32 v142, v142
	v_exp_f32_e32 v143, v143
	v_add_f32_e32 v254, v254, v140
	s_waitcnt lgkmcnt(8)
	v_mfma_f32_32x32x16_bf16 v[32:47], v[172:175], v[180:183], v[32:47]
	v_add_f32_e32 v254, v254, v141
	v_add_f32_e32 v254, v254, v142
	v_add_f32_e32 v254, v254, v143
	v_cvt_pk_bf16_f32 v132, v136, v137
	v_cvt_pk_bf16_f32 v133, v138, v139
	s_waitcnt lgkmcnt(6)
	v_mfma_f32_32x32x16_bf16 v[16:31], v[172:175], v[184:187], v[16:31]
	v_sub_f32_e32 v144, v144, v229
	v_sub_f32_e32 v145, v145, v229
	v_sub_f32_e32 v146, v146, v229
	v_sub_f32_e32 v147, v147, v229
	v_exp_f32_e32 v144, v144
	v_exp_f32_e32 v145, v145
	s_waitcnt lgkmcnt(4)
	v_mfma_f32_32x32x16_bf16 v[0:15], v[172:175], v[188:191], v[0:15]
	v_exp_f32_e32 v146, v146
	v_exp_f32_e32 v147, v147
	v_add_f32_e32 v255, v144, v145
	v_add_f32_e32 v255, v255, v146
	v_add_f32_e32 v255, v255, v147
	s_waitcnt lgkmcnt(2)
	v_mfma_f32_32x32x16_bf16 v[160:175], v[196:199], v[192:195], 0
	v_cvt_pk_bf16_f32 v134, v140, v141
	v_cvt_pk_bf16_f32 v135, v142, v143
	v_sub_f32_e32 v148, v148, v229
	v_sub_f32_e32 v149, v149, v229
	v_sub_f32_e32 v150, v150, v229
	s_waitcnt lgkmcnt(1)
	v_mfma_f32_32x32x16_bf16 v[176:191], v[200:203], v[192:195], 0
	v_add3_u32 v230, v237, v241, s51
	ds_read_b128 v[196:199], v230
	ds_read_b128 v[200:203], v230 offset:8192
	ds_read_b128 v[192:195], v242
	v_sub_f32_e32 v151, v151, v229
	v_exp_f32_e32 v148, v148
	v_exp_f32_e32 v149, v149
	v_exp_f32_e32 v150, v150
	v_exp_f32_e32 v151, v151
	s_waitcnt lgkmcnt(2)
	v_mfma_f32_32x32x16_bf16 v[160:175], v[196:199], v[204:207], v[160:175]
	v_add_f32_e32 v255, v255, v148
	v_add_f32_e32 v255, v255, v149
	v_add_f32_e32 v255, v255, v150
	v_add_f32_e32 v255, v255, v151
	v_cvt_pk_bf16_f32 v136, v144, v145
	s_waitcnt lgkmcnt(1)
	v_mfma_f32_32x32x16_bf16 v[176:191], v[200:203], v[204:207], v[176:191]
	v_add3_u32 v230, v237, v242, s51
	ds_read_b128 v[196:199], v230
	ds_read_b128 v[200:203], v230 offset:8192
	ds_read_b128 v[204:207], v243
	v_cvt_pk_bf16_f32 v137, v146, v147
	v_sub_f32_e32 v152, v152, v229
	v_sub_f32_e32 v153, v153, v229
	v_sub_f32_e32 v154, v154, v229
	v_sub_f32_e32 v155, v155, v229
	s_waitcnt lgkmcnt(2)
	v_mfma_f32_32x32x16_bf16 v[160:175], v[196:199], v[192:195], v[160:175]
	v_exp_f32_e32 v152, v152
	v_exp_f32_e32 v153, v153
	v_exp_f32_e32 v154, v154
	v_exp_f32_e32 v155, v155
	v_add_f32_e32 v255, v255, v152
	s_waitcnt lgkmcnt(1)
	v_mfma_f32_32x32x16_bf16 v[176:191], v[200:203], v[192:195], v[176:191]
	v_add3_u32 v230, v237, v243, s51
	ds_read_b128 v[196:199], v230
	ds_read_b128 v[200:203], v230 offset:8192
	v_add_f32_e32 v255, v255, v153
	v_add_f32_e32 v255, v255, v154
	v_add_f32_e32 v255, v255, v155
	v_cvt_pk_bf16_f32 v138, v148, v149
	v_cvt_pk_bf16_f32 v139, v150, v151
	s_waitcnt lgkmcnt(1)
	v_mfma_f32_32x32x16_bf16 v[160:175], v[196:199], v[204:207], v[160:175]
	v_sub_f32_e32 v156, v156, v229
	v_sub_f32_e32 v157, v157, v229
	v_sub_f32_e32 v158, v158, v229
	v_sub_f32_e32 v159, v159, v229
	v_exp_f32_e32 v156, v156
	s_waitcnt lgkmcnt(0)
	v_mfma_f32_32x32x16_bf16 v[176:191], v[200:203], v[204:207], v[176:191]
	v_exp_f32_e32 v157, v157
	v_exp_f32_e32 v158, v158
	v_exp_f32_e32 v159, v159
	v_add_f32_e32 v255, v255, v156
	v_add_f32_e32 v255, v255, v157
	v_add_f32_e32 v255, v255, v158
	v_add_f32_e32 v255, v255, v159
	v_cvt_pk_bf16_f32 v140, v152, v153
	v_cvt_pk_bf16_f32 v141, v154, v155
	v_cvt_pk_bf16_f32 v142, v156, v157
	v_cvt_pk_bf16_f32 v143, v158, v159
	v_add_f32_e32 v254, v254, v255
	v_mov_b32_e32 v255, v254
	s_nop 1
	v_permlane32_swap_b32_e32 v254, v255
	v_add_f32_e32 v254, v254, v255
	v_fma_f32 v208, v208, v228, v254
	s_branch .Lattn_tail
